# LN2 next-layer block: the two waits after the LDS reads no longer wait for the row's stores (lgkmcnt only)
# speedup vs baseline: 1.0019x; 1.0019x over previous
; #define GAS __attribute__((address_space(1)))
; __device__ __forceinline__ unsigned pk2(float lo, float hi) { const f32x2 v = {lo, hi}; const bf16v2 b = __builtin_convertvector(v, bf16v2); return __builtin_bit_cast(unsigned, b); }
; __device__ __forceinline__ void ph_ln2(Frame& F, int l, int ntok, bool last) {
;     ...
;             __builtin_nontemporal_store((u32x4){pk2(xn[0], xn[1]), pk2(xn[2], xn[3]), pk2(xn[4], xn[5]), pk2(xn[6], xn[7])}, (GAS u32x4*)(xr + cA)); __builtin_nontemporal_store((u32x4){pk2(xn[8], xn[9]), pk2(xn[10], xn[11]), pk2(xn[12], xn[13]), pk2(xn[14], xn[15])}, (GAS u32x4*)(xr + cA + 128));
;             bf16_t* xm = (bf16_t*)(F.ws + WS_XM) + (size_t)row * DM;
;             unsigned w[8];
; #pragma unroll
;             for (int j = 0; j < 4; ++j) { const f32x4 sh = *(const GAS f32x4*)(mdn + LN2_COL(j)), sc = *(const GAS f32x4*)(mdn + 1024 + LN2_COL(j));
;                 w[2 * j] = pk2(xn[4 * j] * (1.f + sc[0]) + sh[0], xn[4 * j + 1] * (1.f + sc[1]) + sh[1]); w[2 * j + 1] = pk2(xn[4 * j + 2] * (1.f + sc[2]) + sh[2], xn[4 * j + 3] * (1.f + sc[3]) + sh[3]); }
;             *(GAS u32x4*)(xm + cA) = (u32x4){w[0], w[1], w[2], w[3]}; *(GAS u32x4*)(xm + cA + 128) = (u32x4){w[4], w[5], w[6], w[7]};
.Lln2_nx_keep:
	ds_read_b128 v[68:71], v173
	ds_read_b128 v[28:31], v173 offset:1024
	ds_read_b128 v[72:75], v173 offset:2048
	s_nop 0
	ds_read_b128 v[76:79], v173 offset:3072
	s_waitcnt lgkmcnt(0)
	v_pk_add_f32 v[76:77], v[76:77], 1.0 op_sel_hi:[1,0]
	s_nop 0
	v_pk_fma_f32 v[28:29], v[16:17], v[76:77], v[28:29]
	v_pk_add_f32 v[76:77], v[78:79], 1.0 op_sel_hi:[1,0]
	v_cvt_pk_bf16_f32 v28, v28, v29
	v_pk_fma_f32 v[30:31], v[18:19], v[76:77], v[30:31]
	s_nop 0
	v_cvt_pk_bf16_f32 v29, v30, v31
	v_pk_add_f32 v[30:31], v[72:73], 1.0 op_sel_hi:[1,0]
	s_nop 0
	v_pk_fma_f32 v[30:31], v[12:13], v[30:31], v[68:69]
	v_pk_add_f32 v[68:69], v[74:75], 1.0 op_sel_hi:[1,0]
	v_cvt_pk_bf16_f32 v30, v30, v31
	v_pk_fma_f32 v[68:69], v[14:15], v[68:69], v[70:71]
	s_nop 0
	v_cvt_pk_bf16_f32 v31, v68, v69
	ds_read_b128 v[68:71], v173 offset:4096
	ds_read_b128 v[72:75], v173 offset:5120
	v_lshl_add_u64 v[80:81], v[38:39], 2, s[36:37]
	ds_read_b128 v[76:79], v173 offset:6144
	s_nop 0
	ds_read_b128 v[80:83], v173 offset:7168
	s_mov_b64 s[36:37], 0
	s_waitcnt lgkmcnt(0)
	v_pk_add_f32 v[80:81], v[80:81], 1.0 op_sel_hi:[1,0]
	s_nop 0
	v_pk_fma_f32 v[72:73], v[24:25], v[80:81], v[72:73]
	v_pk_add_f32 v[80:81], v[82:83], 1.0 op_sel_hi:[1,0]
	v_cvt_pk_bf16_f32 v72, v72, v73
	v_pk_fma_f32 v[74:75], v[26:27], v[80:81], v[74:75]
	s_nop 0
	v_cvt_pk_bf16_f32 v73, v74, v75
	v_pk_add_f32 v[74:75], v[76:77], 1.0 op_sel_hi:[1,0]
	s_nop 0
	v_pk_fma_f32 v[68:69], v[20:21], v[74:75], v[68:69]
	s_nop 0
	v_cvt_pk_bf16_f32 v74, v68, v69
	v_pk_add_f32 v[68:69], v[78:79], 1.0 op_sel_hi:[1,0]
	s_nop 0
	v_pk_fma_f32 v[68:69], v[22:23], v[68:69], v[70:71]
	s_nop 0
	v_cvt_pk_bf16_f32 v75, v68, v69
	v_add_co_u32_e32 v68, vcc, 0x11b00000, v84
	s_nop 1
	v_addc_co_u32_e32 v69, vcc, 0, v85, vcc
	global_store_dwordx4 v[68:69], v[28:31], off
	global_store_dwordx4 v[68:69], v[72:75], off offset:256
